# P8 skinny meta-row epilogue: four k_norm gain loads issued together (were 4 load/vmcnt(0) round trips); on top of v55
# baseline (speedup 1.0000x reference)
.LBB0_1452:
	v_cndmask_b32_e64 v13, 0, 1, s[10:11]
	s_waitcnt vmcnt(0)
	v_pk_mul_f32 v[30:31], v[30:31], v[14:15] op_sel_hi:[1,0]
	v_cmp_ne_u32_e64 s[6:7], 1, v13
	s_andn2_b64 vcc, exec, s[10:11]
	v_pk_mul_f32 v[32:33], v[28:29], v[14:15] op_sel_hi:[1,0]
	s_cbranch_vccnz .LBB0_1454
	global_load_dwordx4 v[36:39], v[10:11], off
	global_load_dwordx4 v[100:103], v[10:11], off offset:64
	global_load_dwordx4 v[104:107], v[10:11], off offset:128
	global_load_dwordx4 v[108:111], v[10:11], off offset:192
	s_waitcnt vmcnt(0)
	v_pk_mul_f32 v[30:31], v[30:31], v[38:39]
	v_pk_mul_f32 v[32:33], v[32:33], v[36:37]
.LBB0_1454:
	s_and_b64 s[20:21], s[10:11], exec
	s_cselect_b32 s21, s27, s59
	s_cselect_b32 s20, s26, s58
	s_add_i32 s22, s14, 0xfffffc00
	s_and_b64 s[10:11], s[10:11], exec
	s_cselect_b32 s10, s14, s22
	v_lshl_add_u64 v[28:29], s[20:21], 0, v[2:3]
	s_ashr_i32 s11, s10, 31
	v_lshl_add_u64 v[28:29], s[10:11], 1, v[28:29]
	v_mov_b32_e32 v13, v3
	v_lshl_add_u64 v[28:29], v[28:29], 0, v[12:13]
	v_bfe_u32 v13, v32, 16, 1
	v_add3_u32 v13, v32, v13, s17
	v_bfe_u32 v32, v33, 16, 1
	v_lshrrev_b32_e32 v13, 16, v13
	v_add3_u32 v32, v33, v32, s17
	v_and_or_b32 v32, v32, s18, v13
	v_bfe_u32 v13, v30, 16, 1
	v_add3_u32 v13, v30, v13, s17
	v_bfe_u32 v30, v31, 16, 1
	v_lshrrev_b32_e32 v13, 16, v13
	v_add3_u32 v30, v31, v30, s17
	v_and_or_b32 v33, v30, s18, v13
	v_add_co_u32_e32 v30, vcc, 0x1020000, v28
	v_mov_b32_e32 v15, v14
	s_nop 0
	v_addc_co_u32_e32 v31, vcc, 0, v29, vcc
	global_store_dwordx2 v[30:31], v[32:33], off sc1
	v_mov_b32_e32 v30, v14
	v_mov_b32_e32 v31, v14
	global_store_dwordx2 v[28:29], v[32:33], off sc1
	v_pk_mul_f32 v[26:27], v[26:27], v[30:31]
	s_and_b64 vcc, exec, s[6:7]
	v_pk_mul_f32 v[32:33], v[24:25], v[14:15]
	s_cbranch_vccnz .LBB0_1456
	v_pk_mul_f32 v[26:27], v[26:27], v[102:103]
	v_pk_mul_f32 v[32:33], v[32:33], v[100:101]
.LBB0_1456:
	s_nop 0
	v_bfe_u32 v13, v32, 16, 1
	v_add3_u32 v13, v32, v13, s17
	v_bfe_u32 v32, v33, 16, 1
	v_lshrrev_b32_e32 v13, 16, v13
	v_add3_u32 v32, v33, v32, s17
	v_and_or_b32 v32, v32, s18, v13
	v_bfe_u32 v13, v26, 16, 1
	v_add3_u32 v13, v26, v13, s17
	v_bfe_u32 v26, v27, 16, 1
	v_lshrrev_b32_e32 v13, 16, v13
	v_add3_u32 v26, v27, v26, s17
	v_lshl_add_u64 v[24:25], v[28:29], 0, s[8:9]
	v_and_or_b32 v33, v26, s18, v13
	v_pk_mul_f32 v[22:23], v[22:23], v[30:31]
	s_and_b64 vcc, exec, s[6:7]
	v_pk_mul_f32 v[20:21], v[20:21], v[14:15]
	global_store_dwordx2 v[28:29], v[32:33], off offset:32 sc1
	global_store_dwordx2 v[24:25], v[32:33], off offset:32 sc1
	s_cbranch_vccnz .LBB0_1458
	v_pk_mul_f32 v[22:23], v[22:23], v[106:107]
	v_pk_mul_f32 v[20:21], v[20:21], v[104:105]
.LBB0_1458:
	s_nop 0
	v_bfe_u32 v13, v20, 16, 1
	v_add3_u32 v13, v20, v13, s17
	v_bfe_u32 v20, v21, 16, 1
	v_lshrrev_b32_e32 v13, 16, v13
	v_add3_u32 v20, v21, v20, s17
	v_and_or_b32 v20, v20, s18, v13
	v_bfe_u32 v13, v22, 16, 1
	v_add3_u32 v13, v22, v13, s17
	v_bfe_u32 v21, v23, 16, 1
	v_lshrrev_b32_e32 v13, 16, v13
	v_add3_u32 v21, v23, v21, s17
	v_and_or_b32 v21, v21, s18, v13
	global_store_dwordx2 v[28:29], v[20:21], off offset:64 sc1
	global_store_dwordx2 v[24:25], v[20:21], off offset:64 sc1
	v_mov_b32_e32 v20, v14
	v_mov_b32_e32 v21, v14
	v_pk_mul_f32 v[18:19], v[18:19], v[20:21]
	s_and_b64 vcc, exec, s[6:7]
	v_pk_mul_f32 v[14:15], v[16:17], v[14:15]
	s_cbranch_vccnz .LBB0_1447
	v_pk_mul_f32 v[18:19], v[18:19], v[110:111]
	v_pk_mul_f32 v[14:15], v[14:15], v[108:109]
	s_branch .LBB0_1447
